# v21 + w_in conversion items reordered so 32 consecutive waves write complete 4 KB output rows
# baseline (speedup 1.0000x reference)
; #define LAS __attribute__((address_space(3)))
; __device__ __forceinline__ void tr_decode(Frame& F, int r, TrItem& t) {
;     constexpr int P_IN = (DM / 128) * (IN_W / 32), P_A = (ATTW / 128) * (DM / 32), P_B = (GMW / 128) * (DM / 32), P_O = (DM / 128) * (DM / 32), P_UP = (DM / 128) * (F2 / 32);
;     const float* W; int Nsrc, nblk, ldk, drow; unsigned char* d8; bf16* db = nullptr; float sc; bool up = false, in = false;
;     if (r < P_IN) { W = F.w_in; Nsrc = IN_W; nblk = IN_W / 32; d8 = (unsigned char*)F.WIN; ldk = DM; sc = 1024.f; in = true; }
;     else if ((r -= P_IN) < P_A) { W = F.w_a; Nsrc = DM; nblk = DM / 32; d8 = (unsigned char*)F.WA; ldk = 2 * ATTW; sc = S_WA; }
;     else if ((r -= P_A) < P_B) { W = F.w_b; Nsrc = DM; nblk = DM / 32; d8 = (unsigned char*)F.WA + ATTW; ldk = 2 * ATTW; sc = S_WB; }
;     else if ((r -= P_B) < P_O) { W = F.w_out; Nsrc = DM; nblk = DM / 32; d8 = (unsigned char*)F.WOUT; ldk = DM; sc = S_WOUT; }
;     else if ((r -= P_O) < P_UP) { W = F.w_up; Nsrc = F2; nblk = F2 / 32; d8 = (unsigned char*)F.WUP; ldk = DM; sc = S_WUP; up = true; }
;     else { r -= P_UP; W = F.w_dn; Nsrc = DM; nblk = DM / 32; d8 = (unsigned char*)F.WDN; ldk = DFF; sc = S_WDN; }
;     const int kb = r / nblk, n = 32 * (r % nblk);
;     drow = n;
;     if (in) { drow = win_dst_row(n); if (n >= SQI && n < SGU) db = F.WINB; }
;     if (up) { const int ch = n < DFF ? n : n - DFF; drow = (ch >> 7) * 256 + (ch & 127) + (n < DFF ? 0 : 128); }
;     t.src = W + (size_t)(128 * kb) * Nsrc + n; t.d8 = d8; t.db = db; t.Nsrc = Nsrc; t.ldk = ldk; t.drow0 = drow; t.k0 = 128 * kb; t.scale = sc;
; template <int LIST> __device__ __forceinline__ void tr_run(Frame& F, int r0, int rend, int stride, LAS float* scr) {
;     TrItem A, B; f32x4 a0[8], a1[8], b0[8], b1[8];
;     int r = r0; bool hasA = r < rend;
;     if (hasA) { tr_decode(F, tr_map<LIST>(r), A); tr_load(A, 0, a0, F.lane); tr_load(A, 1, a1, F.lane); }
.LBB0_24:
	v_readlane_b32 s36, v249, 15
	v_readlane_b32 s4, v249, 40
	v_readlane_b32 s46, v249, 25
	v_readlane_b32 s47, v249, 26
	s_mov_b64 s[0:1], 0x4460
	s_movk_i32 s25, 0x1000
	s_movk_i32 s17, 0x223
	v_readlane_b32 s5, v249, 41
	s_mov_b64 s[10:11], 0
	s_mov_b64 s[6:7], s[46:47]
	s_and_b32 s16, s88, 31
	s_mulk_i32 s16, 0x223
	s_lshr_b32 s17, s88, 5
	s_add_i32 s16, s16, s17
	s_movk_i32 s17, 0x223
	v_readlane_b32 s37, v249, 16
	v_readlane_b32 s38, v249, 17
	v_readlane_b32 s39, v249, 18
	v_readlane_b32 s40, v249, 19
	v_readlane_b32 s41, v249, 20
	v_readlane_b32 s42, v249, 21
	v_readlane_b32 s43, v249, 22
	v_readlane_b32 s44, v249, 23
	v_readlane_b32 s45, v249, 24
	v_readlane_b32 s48, v249, 27
	v_readlane_b32 s49, v249, 28
	v_readlane_b32 s50, v249, 29
	v_readlane_b32 s51, v249, 30
	s_branch .LBB0_40

; __device__ __forceinline__ void tr_decode(Frame& F, int r, TrItem& t) {
;     constexpr int P_IN = (DM / 128) * (IN_W / 32), P_A = (ATTW / 128) * (DM / 32), P_B = (GMW / 128) * (DM / 32), P_O = (DM / 128) * (DM / 32), P_UP = (DM / 128) * (F2 / 32);
;     const float* W; int Nsrc, nblk, ldk, drow; unsigned char* d8; bf16* db = nullptr; float sc; bool up = false, in = false;
;     if (r < P_IN) { W = F.w_in; Nsrc = IN_W; nblk = IN_W / 32; d8 = (unsigned char*)F.WIN; ldk = DM; sc = 1024.f; in = true; }
;     else if ((r -= P_IN) < P_A) { W = F.w_a; Nsrc = DM; nblk = DM / 32; d8 = (unsigned char*)F.WA; ldk = 2 * ATTW; sc = S_WA; }
;     else if ((r -= P_A) < P_B) { W = F.w_b; Nsrc = DM; nblk = DM / 32; d8 = (unsigned char*)F.WA + ATTW; ldk = 2 * ATTW; sc = S_WB; }
;     else if ((r -= P_B) < P_O) { W = F.w_out; Nsrc = DM; nblk = DM / 32; d8 = (unsigned char*)F.WOUT; ldk = DM; sc = S_WOUT; }
;     else if ((r -= P_O) < P_UP) { W = F.w_up; Nsrc = F2; nblk = F2 / 32; d8 = (unsigned char*)F.WUP; ldk = DM; sc = S_WUP; up = true; }
;     else { r -= P_UP; W = F.w_dn; Nsrc = DM; nblk = DM / 32; d8 = (unsigned char*)F.WDN; ldk = DFF; sc = S_WDN; }
;     const int kb = r / nblk, n = 32 * (r % nblk);
;     drow = n;
;     if (in) { drow = win_dst_row(n); if (n >= SQI && n < SGU) db = F.WINB; }
;     if (up) { const int ch = n < DFF ? n : n - DFF; drow = (ch >> 7) * 256 + (ch & 127) + (n < DFF ? 0 : 128); }
;     t.src = W + (size_t)(128 * kb) * Nsrc + n; t.d8 = d8; t.db = db; t.Nsrc = Nsrc; t.ldk = ldk; t.drow0 = drow; t.k0 = 128 * kb; t.scale = sc;
; template <int LIST> __device__ __forceinline__ void tr_run(Frame& F, int r0, int rend, int stride, LAS float* scr) {
;     ...
;         r = rb + stride; hasA = r < rend;
;         if (hasA) { tr_decode(F, tr_map<LIST>(r), A); tr_load(A, 0, a0, F.lane); tr_load(A, 1, a1, F.lane); }
.LBB0_68:
	v_readlane_b32 s56, v249, 15
	v_readlane_b32 s10, v249, 40
	v_readlane_b32 s66, v249, 25
	v_readlane_b32 s67, v249, 26
	s_mov_b64 s[0:1], 0x4460
	s_movk_i32 s31, 0x1000
	s_movk_i32 s35, 0x223
	v_readlane_b32 s11, v249, 41
	s_mov_b64 s[20:21], 0
	s_mov_b64 s[16:17], s[66:67]
	s_and_b32 s34, s36, 31
	s_mulk_i32 s34, 0x223
	s_lshr_b32 s35, s36, 5
	s_add_i32 s34, s34, s35
	s_movk_i32 s35, 0x223
	v_readlane_b32 s57, v249, 16
	v_readlane_b32 s58, v249, 17
	v_readlane_b32 s59, v249, 18
	v_readlane_b32 s60, v249, 19
	v_readlane_b32 s61, v249, 20
	v_readlane_b32 s62, v249, 21
	v_readlane_b32 s63, v249, 22
	v_readlane_b32 s64, v249, 23
	v_readlane_b32 s65, v249, 24
	v_readlane_b32 s68, v249, 27
	v_readlane_b32 s69, v249, 28
	v_readlane_b32 s70, v249, 29
	v_readlane_b32 s71, v249, 30
	s_branch .LBB0_77

; __device__ __forceinline__ void tr_decode(Frame& F, int r, TrItem& t) {
;     constexpr int P_IN = (DM / 128) * (IN_W / 32), P_A = (ATTW / 128) * (DM / 32), P_B = (GMW / 128) * (DM / 32), P_O = (DM / 128) * (DM / 32), P_UP = (DM / 128) * (F2 / 32);
;     const float* W; int Nsrc, nblk, ldk, drow; unsigned char* d8; bf16* db = nullptr; float sc; bool up = false, in = false;
;     if (r < P_IN) { W = F.w_in; Nsrc = IN_W; nblk = IN_W / 32; d8 = (unsigned char*)F.WIN; ldk = DM; sc = 1024.f; in = true; }
;     else if ((r -= P_IN) < P_A) { W = F.w_a; Nsrc = DM; nblk = DM / 32; d8 = (unsigned char*)F.WA; ldk = 2 * ATTW; sc = S_WA; }
;     else if ((r -= P_A) < P_B) { W = F.w_b; Nsrc = DM; nblk = DM / 32; d8 = (unsigned char*)F.WA + ATTW; ldk = 2 * ATTW; sc = S_WB; }
;     else if ((r -= P_B) < P_O) { W = F.w_out; Nsrc = DM; nblk = DM / 32; d8 = (unsigned char*)F.WOUT; ldk = DM; sc = S_WOUT; }
;     else if ((r -= P_O) < P_UP) { W = F.w_up; Nsrc = F2; nblk = F2 / 32; d8 = (unsigned char*)F.WUP; ldk = DM; sc = S_WUP; up = true; }
;     else { r -= P_UP; W = F.w_dn; Nsrc = DM; nblk = DM / 32; d8 = (unsigned char*)F.WDN; ldk = DFF; sc = S_WDN; }
;     const int kb = r / nblk, n = 32 * (r % nblk);
;     drow = n;
;     if (in) { drow = win_dst_row(n); if (n >= SQI && n < SGU) db = F.WINB; }
;     if (up) { const int ch = n < DFF ? n : n - DFF; drow = (ch >> 7) * 256 + (ch & 127) + (n < DFF ? 0 : 128); }
;     t.src = W + (size_t)(128 * kb) * Nsrc + n; t.d8 = d8; t.db = db; t.Nsrc = Nsrc; t.ldk = ldk; t.drow0 = drow; t.k0 = 128 * kb; t.scale = sc;
; template <int LIST> __device__ __forceinline__ void tr_run(Frame& F, int r0, int rend, int stride, LAS float* scr) {
;     ...
;         const int rb = r + stride; const bool hasB = rb < rend;
;         if (hasB) { tr_decode(F, tr_map<LIST>(rb), B); tr_load(B, 0, b0, F.lane); tr_load(B, 1, b1, F.lane); }
.LBB0_116:
	v_readlane_b32 s36, v249, 15
	v_readlane_b32 s4, v249, 40
	v_readlane_b32 s46, v249, 25
	v_readlane_b32 s47, v249, 26
	s_mov_b64 s[0:1], 0x4460
	s_movk_i32 s25, 0x1000
	s_movk_i32 s33, 0x223
	v_readlane_b32 s5, v249, 41
	s_mov_b64 s[20:21], 0
	s_mov_b64 s[16:17], s[46:47]
	s_and_b32 s30, s27, 31
	s_mulk_i32 s30, 0x223
	s_lshr_b32 s33, s27, 5
	s_add_i32 s30, s30, s33
	s_movk_i32 s33, 0x223
	v_readlane_b32 s37, v249, 16
	v_readlane_b32 s38, v249, 17
	v_readlane_b32 s39, v249, 18
	v_readlane_b32 s40, v249, 19
	v_readlane_b32 s41, v249, 20
	v_readlane_b32 s42, v249, 21
	v_readlane_b32 s43, v249, 22
	v_readlane_b32 s44, v249, 23
	v_readlane_b32 s45, v249, 24
	v_readlane_b32 s48, v249, 27
	v_readlane_b32 s49, v249, 28
	v_readlane_b32 s50, v249, 29
	v_readlane_b32 s51, v249, 30
	s_branch .LBB0_127
